# v33 + hand-written in-place merge epilogue (proj phase), back-edge register rotation movs removed
# speedup vs baseline: 1.0031x; 1.0031x over previous
;     __device__ bool next(int i, Unit& u) const { if (!base.next(i >> 1, u)) return false; if (i & 1) { u.pm += MTOK / BM; u.pn += DM / BM; } return true; }
;   __device__ __forceinline__ bool next(int i,AttnUnit&u)const{ if(i>=2||vcu>=256)return false; const int s=vcu&3; u.bh=vcu>>2; u.qb=(i==0)?7-s:s; return true; }
; template <class Epi, class Sched, bool ALIGN_EPI = false, bool SP2 = false>
; __device__ __forceinline__ void gemm_phase(PG8_LAS unsigned char* lds, const Gemm g, const Sched& S, const Epi& E) {
;     ...
;     for (;;) {
;         const bool has_next = S.next(ui + 1, nxt);
;         const char* nA = has_next ? (const char*)g.A + (size_t)nxt.pm * tstep + (nxt.half == 2 ? hstep : (size_t)0) : cA; const char* nB = has_next ? (const char*)g.Bt + (size_t)nxt.pn * tstep : cB;
;     ...
;         cur = nxt; cA = nA; cB = nB; ++ui;
.LBB0_1127:
	s_andn2_b64 vcc, exec, s[0:1]
	s_mov_b32 s0, s38
	s_mov_b32 s4, s18
	s_mov_b64 s[14:15], s[58:59]
	s_mov_b64 s[6:7], s[56:57]
	s_mov_b32 s1, s41
	s_cbranch_vccz .LBB0_1205

;     __device__ __forceinline__ void operator()(f32x4 (&acc)[2][2][4][2], const Unit& u, int wr, int wc, int fr, int fq) const {
;         const bool second = u.pn >= DM / BM; const int pm = second ? u.pm - MTOK / BM : u.pm, pn = second ? u.pn - DM / BM : u.pn;
;         const int row0 = pm * BM + wr * 64 + fr, col0 = pn * BM + wc * 32 + 8 * fq;
;         const unsigned char* GAx = second ? GB : GA; const size_t amask = second ? (size_t)0 : ~(size_t)0;
;         u32x2 ga[2][2][2], gb[2][2][2];
;     ...
;         MG_LOAD(0, 0); MG_LOAD(1, 1);
;         asm volatile("" ::: "memory");
; #pragma unroll
;         for (int c = 0; c < 4; ++c) { const int ai = c >> 1;
; #pragma unroll
;             for (int m2 = 0; m2 < 2; ++m2) { const int m = 2 * (c & 1) + m2;
; #pragma unroll
;                 for (int bj = 0; bj < 2; ++bj) { const u32x2 a2 = ga[c & 1][m2][bj], b2 = gb[c & 1][m2][bj]; const float q = 1.0f / 255.0f;
;                     const f32x4 sa0 = {(float)((a2.x >> 0) & 0xffu), (float)((a2.x >> 8) & 0xffu), (float)((a2.x >> 16) & 0xffu), (float)((a2.x >> 24) & 0xffu)};
;                     const f32x4 sa1 = {(float)((a2.y >> 0) & 0xffu), (float)((a2.y >> 8) & 0xffu), (float)((a2.y >> 16) & 0xffu), (float)((a2.y >> 24) & 0xffu)};
;                     f32x4 sb0 = {(float)((b2.x >> 0) & 0xffu), (float)((b2.x >> 8) & 0xffu), (float)((b2.x >> 16) & 0xffu), (float)((b2.x >> 24) & 0xffu)};
;                     f32x4 sb1 = {(float)((b2.y >> 0) & 0xffu), (float)((b2.y >> 8) & 0xffu), (float)((b2.y >> 16) & 0xffu), (float)((b2.y >> 24) & 0xffu)};
; #pragma unroll
;                     for (int e = 0; e < 4; ++e) { sb0[e] = fmaxf(sb0[e], 2.55e-4f); sb1[e] = fmaxf(sb1[e], 2.55e-4f); }
;                     if (second) *(u32x4*)(MERGED + (size_t)(row0 + ai * HALF + m * 16) * DM + col0 + bj * HALF) = pack8(acc[ai][bj][m][0] * (sb0 * q), acc[ai][bj][m][1] * (sb1 * q));
;                     if (!second) { f32x4 r0, r1;
; #pragma unroll
;                         for (int e = 0; e < 4; ++e) { r0[e] = sa0[e] * __builtin_amdgcn_rcpf(sb0[e]); r1[e] = sa1[e] * __builtin_amdgcn_rcpf(sb1[e]); }
;                         acc[ai][bj][m][0] = acc[ai][bj][m][0] * r0; acc[ai][bj][m][1] = acc[ai][bj][m][1] * r1; }
.LBB0_1138:
	s_cmp_gt_i32 s0, 3
	s_cbranch_scc1 .Lmg_second
	s_lshl_b32 s1, s4, 8
	s_lshl_b32 s5, s0, 8
	v_add_u32_e32 v253, s1, v200
	v_or_b32_e32 v252, s5, v202
	v_lshl_add_u32 v252, v253, 10, v252
	global_load_dwordx2 v[36:37], v252, s[10:11]
	global_load_dwordx2 v[40:41], v252, s[34:35]
	global_load_dwordx2 v[38:39], v252, s[10:11] offset:128
	global_load_dwordx2 v[42:43], v252, s[34:35] offset:128
	v_add_u32_e32 v252, 0x4000, v252
	global_load_dwordx2 v[68:69], v252, s[10:11]
	global_load_dwordx2 v[72:73], v252, s[34:35]
	global_load_dwordx2 v[70:71], v252, s[10:11] offset:128
	global_load_dwordx2 v[74:75], v252, s[34:35] offset:128
	v_add_u32_e32 v252, 0x4000, v252
	global_load_dwordx2 v[100:101], v252, s[10:11]
	global_load_dwordx2 v[104:105], v252, s[34:35]
	global_load_dwordx2 v[102:103], v252, s[10:11] offset:128
	global_load_dwordx2 v[106:107], v252, s[34:35] offset:128
	v_add_u32_e32 v252, 0x4000, v252
	global_load_dwordx2 v[132:133], v252, s[10:11]
	global_load_dwordx2 v[136:137], v252, s[34:35]
	global_load_dwordx2 v[134:135], v252, s[10:11] offset:128
	global_load_dwordx2 v[138:139], v252, s[34:35] offset:128
	v_add_u32_e32 v252, 0x14000, v252
	global_load_dwordx2 v[174:175], v252, s[10:11]
	global_load_dwordx2 v[178:179], v252, s[34:35]
	global_load_dwordx2 v[176:177], v252, s[10:11] offset:128
	global_load_dwordx2 v[180:181], v252, s[34:35] offset:128
	v_add_u32_e32 v252, 0x4000, v252
	global_load_dwordx2 v[182:183], v252, s[10:11]
	global_load_dwordx2 v[186:187], v252, s[34:35]
	global_load_dwordx2 v[184:185], v252, s[10:11] offset:128
	global_load_dwordx2 v[188:189], v252, s[34:35] offset:128
	v_add_u32_e32 v252, 0x4000, v252
	global_load_dwordx2 v[190:191], v252, s[10:11]
	global_load_dwordx2 v[194:195], v252, s[34:35]
	global_load_dwordx2 v[192:193], v252, s[10:11] offset:128
	global_load_dwordx2 v[196:197], v252, s[34:35] offset:128
	v_add_u32_e32 v252, 0x4000, v252
	global_load_dwordx2 v[204:205], v252, s[10:11]
	global_load_dwordx2 v[208:209], v252, s[34:35]
	global_load_dwordx2 v[206:207], v252, s[10:11] offset:128
	global_load_dwordx2 v[210:211], v252, s[34:35] offset:128
	s_waitcnt vmcnt(30)
	v_cvt_f32_ubyte0_e32 v228, v36
	v_cvt_f32_ubyte1_e32 v229, v36
	v_cvt_f32_ubyte2_e32 v230, v36
	v_cvt_f32_ubyte3_e32 v231, v36
	v_cvt_f32_ubyte0_e32 v232, v37
	v_cvt_f32_ubyte1_e32 v233, v37
	v_cvt_f32_ubyte2_e32 v234, v37
	v_cvt_f32_ubyte3_e32 v235, v37
	v_max_f32_e32 v228, 0x3985b185, v228
	v_max_f32_e32 v229, 0x3985b185, v229
	v_max_f32_e32 v230, 0x3985b185, v230
	v_max_f32_e32 v231, 0x3985b185, v231
	v_max_f32_e32 v232, 0x3985b185, v232
	v_max_f32_e32 v233, 0x3985b185, v233
	v_max_f32_e32 v234, 0x3985b185, v234
	v_max_f32_e32 v235, 0x3985b185, v235
	v_rcp_f32_e32 v228, v228
	v_rcp_f32_e32 v229, v229
	v_rcp_f32_e32 v230, v230
	v_rcp_f32_e32 v231, v231
	v_rcp_f32_e32 v232, v232
	v_rcp_f32_e32 v233, v233
	v_rcp_f32_e32 v234, v234
	v_rcp_f32_e32 v235, v235
	v_cvt_f32_ubyte0_e32 v236, v40
	v_cvt_f32_ubyte1_e32 v237, v40
	v_cvt_f32_ubyte2_e32 v238, v40
	v_cvt_f32_ubyte3_e32 v239, v40
	v_cvt_f32_ubyte0_e32 v240, v41
	v_cvt_f32_ubyte1_e32 v241, v41
	v_cvt_f32_ubyte2_e32 v242, v41
	v_cvt_f32_ubyte3_e32 v243, v41
	v_pk_mul_f32 v[228:229], v[228:229], v[236:237]
	v_pk_mul_f32 v[230:231], v[230:231], v[238:239]
	v_pk_mul_f32 v[232:233], v[232:233], v[240:241]
	v_pk_mul_f32 v[234:235], v[234:235], v[242:243]
	v_pk_mul_f32 v[56:57], v[56:57], v[228:229]
	v_pk_mul_f32 v[58:59], v[58:59], v[230:231]
	v_pk_mul_f32 v[52:53], v[52:53], v[232:233]
	v_pk_mul_f32 v[54:55], v[54:55], v[234:235]
	s_waitcnt vmcnt(28)
	v_cvt_f32_ubyte0_e32 v228, v38
	v_cvt_f32_ubyte1_e32 v229, v38
	v_cvt_f32_ubyte2_e32 v230, v38
	v_cvt_f32_ubyte3_e32 v231, v38
	v_cvt_f32_ubyte0_e32 v232, v39
	v_cvt_f32_ubyte1_e32 v233, v39
	v_cvt_f32_ubyte2_e32 v234, v39
	v_cvt_f32_ubyte3_e32 v235, v39
	v_max_f32_e32 v228, 0x3985b185, v228
	v_max_f32_e32 v229, 0x3985b185, v229
	v_max_f32_e32 v230, 0x3985b185, v230
	v_max_f32_e32 v231, 0x3985b185, v231
	v_max_f32_e32 v232, 0x3985b185, v232
	v_max_f32_e32 v233, 0x3985b185, v233
	v_max_f32_e32 v234, 0x3985b185, v234
	v_max_f32_e32 v235, 0x3985b185, v235
	v_rcp_f32_e32 v228, v228
	v_rcp_f32_e32 v229, v229
	v_rcp_f32_e32 v230, v230
	v_rcp_f32_e32 v231, v231
	v_rcp_f32_e32 v232, v232
	v_rcp_f32_e32 v233, v233
	v_rcp_f32_e32 v234, v234
	v_rcp_f32_e32 v235, v235
	v_cvt_f32_ubyte0_e32 v236, v42
	v_cvt_f32_ubyte1_e32 v237, v42
	v_cvt_f32_ubyte2_e32 v238, v42
	v_cvt_f32_ubyte3_e32 v239, v42
	v_cvt_f32_ubyte0_e32 v240, v43
	v_cvt_f32_ubyte1_e32 v241, v43
	v_cvt_f32_ubyte2_e32 v242, v43
	v_cvt_f32_ubyte3_e32 v243, v43
	v_pk_mul_f32 v[228:229], v[228:229], v[236:237]
	v_pk_mul_f32 v[230:231], v[230:231], v[238:239]
	v_pk_mul_f32 v[232:233], v[232:233], v[240:241]
	v_pk_mul_f32 v[234:235], v[234:235], v[242:243]
	v_pk_mul_f32 v[160:161], v[160:161], v[228:229]
	v_pk_mul_f32 v[162:163], v[162:163], v[230:231]
	v_pk_mul_f32 v[156:157], v[156:157], v[232:233]
	v_pk_mul_f32 v[158:159], v[158:159], v[234:235]
	s_waitcnt vmcnt(26)
; __device__ __forceinline__ u32x4 pack8(const f32x4 a, const f32x4 b) { u32x4 w; w.x = cvt_pk_bf16(a[0], a[1]); w.y = cvt_pk_bf16(a[2], a[3]); w.z = cvt_pk_bf16(b[0], b[1]); w.w = cvt_pk_bf16(b[2], b[3]); return w; }
;     __device__ __forceinline__ void operator()(f32x4 (&acc)[2][2][4][2], const Unit& u, int wr, int wc, int fr, int fq) const {
;     ...
;                 for (int bj = 0; bj < 2; ++bj) { const u32x2 a2 = ga[c & 1][m2][bj], b2 = gb[c & 1][m2][bj]; const float q = 1.0f / 255.0f;
;                     const f32x4 sa0 = {(float)((a2.x >> 0) & 0xffu), (float)((a2.x >> 8) & 0xffu), (float)((a2.x >> 16) & 0xffu), (float)((a2.x >> 24) & 0xffu)};
;                     const f32x4 sa1 = {(float)((a2.y >> 0) & 0xffu), (float)((a2.y >> 8) & 0xffu), (float)((a2.y >> 16) & 0xffu), (float)((a2.y >> 24) & 0xffu)};
;                     f32x4 sb0 = {(float)((b2.x >> 0) & 0xffu), (float)((b2.x >> 8) & 0xffu), (float)((b2.x >> 16) & 0xffu), (float)((b2.x >> 24) & 0xffu)};
;                     f32x4 sb1 = {(float)((b2.y >> 0) & 0xffu), (float)((b2.y >> 8) & 0xffu), (float)((b2.y >> 16) & 0xffu), (float)((b2.y >> 24) & 0xffu)};
; #pragma unroll
;                     for (int e = 0; e < 4; ++e) { sb0[e] = fmaxf(sb0[e], 2.55e-4f); sb1[e] = fmaxf(sb1[e], 2.55e-4f); }
;                     if (second) *(u32x4*)(MERGED + (size_t)(row0 + ai * HALF + m * 16) * DM + col0 + bj * HALF) = pack8(acc[ai][bj][m][0] * (sb0 * q), acc[ai][bj][m][1] * (sb1 * q));
;                     if (!second) { f32x4 r0, r1;
; #pragma unroll
;                         for (int e = 0; e < 4; ++e) { r0[e] = sa0[e] * __builtin_amdgcn_rcpf(sb0[e]); r1[e] = sa1[e] * __builtin_amdgcn_rcpf(sb1[e]); }
;                         acc[ai][bj][m][0] = acc[ai][bj][m][0] * r0; acc[ai][bj][m][1] = acc[ai][bj][m][1] * r1; }
	v_cvt_f32_ubyte0_e32 v228, v68
	v_cvt_f32_ubyte1_e32 v229, v68
	v_cvt_f32_ubyte2_e32 v230, v68
	v_cvt_f32_ubyte3_e32 v231, v68
	v_cvt_f32_ubyte0_e32 v232, v69
	v_cvt_f32_ubyte1_e32 v233, v69
	v_cvt_f32_ubyte2_e32 v234, v69
	v_cvt_f32_ubyte3_e32 v235, v69
	v_max_f32_e32 v228, 0x3985b185, v228
	v_max_f32_e32 v229, 0x3985b185, v229
	v_max_f32_e32 v230, 0x3985b185, v230
	v_max_f32_e32 v231, 0x3985b185, v231
	v_max_f32_e32 v232, 0x3985b185, v232
	v_max_f32_e32 v233, 0x3985b185, v233
	v_max_f32_e32 v234, 0x3985b185, v234
	v_max_f32_e32 v235, 0x3985b185, v235
	v_rcp_f32_e32 v228, v228
	v_rcp_f32_e32 v229, v229
	v_rcp_f32_e32 v230, v230
	v_rcp_f32_e32 v231, v231
	v_rcp_f32_e32 v232, v232
	v_rcp_f32_e32 v233, v233
	v_rcp_f32_e32 v234, v234
	v_rcp_f32_e32 v235, v235
	v_cvt_f32_ubyte0_e32 v236, v72
	v_cvt_f32_ubyte1_e32 v237, v72
	v_cvt_f32_ubyte2_e32 v238, v72
	v_cvt_f32_ubyte3_e32 v239, v72
	v_cvt_f32_ubyte0_e32 v240, v73
	v_cvt_f32_ubyte1_e32 v241, v73
	v_cvt_f32_ubyte2_e32 v242, v73
	v_cvt_f32_ubyte3_e32 v243, v73
	v_pk_mul_f32 v[228:229], v[228:229], v[236:237]
	v_pk_mul_f32 v[230:231], v[230:231], v[238:239]
	v_pk_mul_f32 v[232:233], v[232:233], v[240:241]
	v_pk_mul_f32 v[234:235], v[234:235], v[242:243]
	v_pk_mul_f32 v[88:89], v[88:89], v[228:229]
	v_pk_mul_f32 v[90:91], v[90:91], v[230:231]
	v_pk_mul_f32 v[84:85], v[84:85], v[232:233]
	v_pk_mul_f32 v[86:87], v[86:87], v[234:235]
	s_waitcnt vmcnt(24)
	v_cvt_f32_ubyte0_e32 v228, v70
	v_cvt_f32_ubyte1_e32 v229, v70
	v_cvt_f32_ubyte2_e32 v230, v70
	v_cvt_f32_ubyte3_e32 v231, v70
	v_cvt_f32_ubyte0_e32 v232, v71
	v_cvt_f32_ubyte1_e32 v233, v71
	v_cvt_f32_ubyte2_e32 v234, v71
	v_cvt_f32_ubyte3_e32 v235, v71
	v_max_f32_e32 v228, 0x3985b185, v228
	v_max_f32_e32 v229, 0x3985b185, v229
	v_max_f32_e32 v230, 0x3985b185, v230
	v_max_f32_e32 v231, 0x3985b185, v231
	v_max_f32_e32 v232, 0x3985b185, v232
	v_max_f32_e32 v233, 0x3985b185, v233
	v_max_f32_e32 v234, 0x3985b185, v234
	v_max_f32_e32 v235, 0x3985b185, v235
	v_rcp_f32_e32 v228, v228
	v_rcp_f32_e32 v229, v229
	v_rcp_f32_e32 v230, v230
	v_rcp_f32_e32 v231, v231
	v_rcp_f32_e32 v232, v232
	v_rcp_f32_e32 v233, v233
	v_rcp_f32_e32 v234, v234
	v_rcp_f32_e32 v235, v235
	v_cvt_f32_ubyte0_e32 v236, v74
	v_cvt_f32_ubyte1_e32 v237, v74
	v_cvt_f32_ubyte2_e32 v238, v74
	v_cvt_f32_ubyte3_e32 v239, v74
	v_cvt_f32_ubyte0_e32 v240, v75
	v_cvt_f32_ubyte1_e32 v241, v75
	v_cvt_f32_ubyte2_e32 v242, v75
	v_cvt_f32_ubyte3_e32 v243, v75
	v_pk_mul_f32 v[228:229], v[228:229], v[236:237]
	v_pk_mul_f32 v[230:231], v[230:231], v[238:239]
	v_pk_mul_f32 v[232:233], v[232:233], v[240:241]
	v_pk_mul_f32 v[234:235], v[234:235], v[242:243]
	v_pk_mul_f32 v[152:153], v[152:153], v[228:229]
	v_pk_mul_f32 v[154:155], v[154:155], v[230:231]
	v_pk_mul_f32 v[148:149], v[148:149], v[232:233]
	v_pk_mul_f32 v[150:151], v[150:151], v[234:235]
	s_waitcnt vmcnt(22)
	v_cvt_f32_ubyte0_e32 v228, v100
	v_cvt_f32_ubyte1_e32 v229, v100
	v_cvt_f32_ubyte2_e32 v230, v100
	v_cvt_f32_ubyte3_e32 v231, v100
	v_cvt_f32_ubyte0_e32 v232, v101
	v_cvt_f32_ubyte1_e32 v233, v101
	v_cvt_f32_ubyte2_e32 v234, v101
	v_cvt_f32_ubyte3_e32 v235, v101
	v_max_f32_e32 v228, 0x3985b185, v228
	v_max_f32_e32 v229, 0x3985b185, v229
	v_max_f32_e32 v230, 0x3985b185, v230
	v_max_f32_e32 v231, 0x3985b185, v231
	v_max_f32_e32 v232, 0x3985b185, v232
	v_max_f32_e32 v233, 0x3985b185, v233
	v_max_f32_e32 v234, 0x3985b185, v234
	v_max_f32_e32 v235, 0x3985b185, v235
	v_rcp_f32_e32 v228, v228
	v_rcp_f32_e32 v229, v229
	v_rcp_f32_e32 v230, v230
	v_rcp_f32_e32 v231, v231
	v_rcp_f32_e32 v232, v232
	v_rcp_f32_e32 v233, v233
	v_rcp_f32_e32 v234, v234
	v_rcp_f32_e32 v235, v235
	v_cvt_f32_ubyte0_e32 v236, v104
	v_cvt_f32_ubyte1_e32 v237, v104
	v_cvt_f32_ubyte2_e32 v238, v104
	v_cvt_f32_ubyte3_e32 v239, v104
	v_cvt_f32_ubyte0_e32 v240, v105
	v_cvt_f32_ubyte1_e32 v241, v105
	v_cvt_f32_ubyte2_e32 v242, v105
	v_cvt_f32_ubyte3_e32 v243, v105
	v_pk_mul_f32 v[228:229], v[228:229], v[236:237]
	v_pk_mul_f32 v[230:231], v[230:231], v[238:239]
	v_pk_mul_f32 v[232:233], v[232:233], v[240:241]
	v_pk_mul_f32 v[234:235], v[234:235], v[242:243]
	v_pk_mul_f32 v[120:121], v[120:121], v[228:229]
	v_pk_mul_f32 v[122:123], v[122:123], v[230:231]
	v_pk_mul_f32 v[116:117], v[116:117], v[232:233]
	v_pk_mul_f32 v[118:119], v[118:119], v[234:235]
	s_waitcnt vmcnt(20)
	v_cvt_f32_ubyte0_e32 v228, v102
	v_cvt_f32_ubyte1_e32 v229, v102
	v_cvt_f32_ubyte2_e32 v230, v102
	v_cvt_f32_ubyte3_e32 v231, v102
	v_cvt_f32_ubyte0_e32 v232, v103
	v_cvt_f32_ubyte1_e32 v233, v103
	v_cvt_f32_ubyte2_e32 v234, v103
	v_cvt_f32_ubyte3_e32 v235, v103
	v_max_f32_e32 v228, 0x3985b185, v228
	v_max_f32_e32 v229, 0x3985b185, v229
	v_max_f32_e32 v230, 0x3985b185, v230
	v_max_f32_e32 v231, 0x3985b185, v231
	v_max_f32_e32 v232, 0x3985b185, v232
	v_max_f32_e32 v233, 0x3985b185, v233
	v_max_f32_e32 v234, 0x3985b185, v234
	v_max_f32_e32 v235, 0x3985b185, v235
	v_rcp_f32_e32 v228, v228
	v_rcp_f32_e32 v229, v229
	v_rcp_f32_e32 v230, v230
	v_rcp_f32_e32 v231, v231
	v_rcp_f32_e32 v232, v232
	v_rcp_f32_e32 v233, v233
	v_rcp_f32_e32 v234, v234
	v_rcp_f32_e32 v235, v235
	v_cvt_f32_ubyte0_e32 v236, v106
	v_cvt_f32_ubyte1_e32 v237, v106
	v_cvt_f32_ubyte2_e32 v238, v106
	v_cvt_f32_ubyte3_e32 v239, v106
	v_cvt_f32_ubyte0_e32 v240, v107
	v_cvt_f32_ubyte1_e32 v241, v107
	v_cvt_f32_ubyte2_e32 v242, v107
	v_cvt_f32_ubyte3_e32 v243, v107
	v_pk_mul_f32 v[228:229], v[228:229], v[236:237]
	v_pk_mul_f32 v[230:231], v[230:231], v[238:239]
	v_pk_mul_f32 v[232:233], v[232:233], v[240:241]
	v_pk_mul_f32 v[234:235], v[234:235], v[242:243]
	v_pk_mul_f32 v[144:145], v[144:145], v[228:229]
	v_pk_mul_f32 v[146:147], v[146:147], v[230:231]
	v_pk_mul_f32 v[140:141], v[140:141], v[232:233]
	v_pk_mul_f32 v[142:143], v[142:143], v[234:235]
	s_waitcnt vmcnt(18)
; __device__ __forceinline__ u32x4 pack8(const f32x4 a, const f32x4 b) { u32x4 w; w.x = cvt_pk_bf16(a[0], a[1]); w.y = cvt_pk_bf16(a[2], a[3]); w.z = cvt_pk_bf16(b[0], b[1]); w.w = cvt_pk_bf16(b[2], b[3]); return w; }
;     __device__ __forceinline__ void operator()(f32x4 (&acc)[2][2][4][2], const Unit& u, int wr, int wc, int fr, int fq) const {
;     ...
;                 for (int bj = 0; bj < 2; ++bj) { const u32x2 a2 = ga[c & 1][m2][bj], b2 = gb[c & 1][m2][bj]; const float q = 1.0f / 255.0f;
;                     const f32x4 sa0 = {(float)((a2.x >> 0) & 0xffu), (float)((a2.x >> 8) & 0xffu), (float)((a2.x >> 16) & 0xffu), (float)((a2.x >> 24) & 0xffu)};
;                     const f32x4 sa1 = {(float)((a2.y >> 0) & 0xffu), (float)((a2.y >> 8) & 0xffu), (float)((a2.y >> 16) & 0xffu), (float)((a2.y >> 24) & 0xffu)};
;                     f32x4 sb0 = {(float)((b2.x >> 0) & 0xffu), (float)((b2.x >> 8) & 0xffu), (float)((b2.x >> 16) & 0xffu), (float)((b2.x >> 24) & 0xffu)};
;                     f32x4 sb1 = {(float)((b2.y >> 0) & 0xffu), (float)((b2.y >> 8) & 0xffu), (float)((b2.y >> 16) & 0xffu), (float)((b2.y >> 24) & 0xffu)};
; #pragma unroll
;                     for (int e = 0; e < 4; ++e) { sb0[e] = fmaxf(sb0[e], 2.55e-4f); sb1[e] = fmaxf(sb1[e], 2.55e-4f); }
;                     if (second) *(u32x4*)(MERGED + (size_t)(row0 + ai * HALF + m * 16) * DM + col0 + bj * HALF) = pack8(acc[ai][bj][m][0] * (sb0 * q), acc[ai][bj][m][1] * (sb1 * q));
;                     if (!second) { f32x4 r0, r1;
; #pragma unroll
;                         for (int e = 0; e < 4; ++e) { r0[e] = sa0[e] * __builtin_amdgcn_rcpf(sb0[e]); r1[e] = sa1[e] * __builtin_amdgcn_rcpf(sb1[e]); }
;                         acc[ai][bj][m][0] = acc[ai][bj][m][0] * r0; acc[ai][bj][m][1] = acc[ai][bj][m][1] * r1; }
	v_cvt_f32_ubyte0_e32 v228, v132
	v_cvt_f32_ubyte1_e32 v229, v132
	v_cvt_f32_ubyte2_e32 v230, v132
	v_cvt_f32_ubyte3_e32 v231, v132
	v_cvt_f32_ubyte0_e32 v232, v133
	v_cvt_f32_ubyte1_e32 v233, v133
	v_cvt_f32_ubyte2_e32 v234, v133
	v_cvt_f32_ubyte3_e32 v235, v133
	v_max_f32_e32 v228, 0x3985b185, v228
	v_max_f32_e32 v229, 0x3985b185, v229
	v_max_f32_e32 v230, 0x3985b185, v230
	v_max_f32_e32 v231, 0x3985b185, v231
	v_max_f32_e32 v232, 0x3985b185, v232
	v_max_f32_e32 v233, 0x3985b185, v233
	v_max_f32_e32 v234, 0x3985b185, v234
	v_max_f32_e32 v235, 0x3985b185, v235
	v_rcp_f32_e32 v228, v228
	v_rcp_f32_e32 v229, v229
	v_rcp_f32_e32 v230, v230
	v_rcp_f32_e32 v231, v231
	v_rcp_f32_e32 v232, v232
	v_rcp_f32_e32 v233, v233
	v_rcp_f32_e32 v234, v234
	v_rcp_f32_e32 v235, v235
	v_cvt_f32_ubyte0_e32 v236, v136
	v_cvt_f32_ubyte1_e32 v237, v136
	v_cvt_f32_ubyte2_e32 v238, v136
	v_cvt_f32_ubyte3_e32 v239, v136
	v_cvt_f32_ubyte0_e32 v240, v137
	v_cvt_f32_ubyte1_e32 v241, v137
	v_cvt_f32_ubyte2_e32 v242, v137
	v_cvt_f32_ubyte3_e32 v243, v137
	v_pk_mul_f32 v[228:229], v[228:229], v[236:237]
	v_pk_mul_f32 v[230:231], v[230:231], v[238:239]
	v_pk_mul_f32 v[232:233], v[232:233], v[240:241]
	v_pk_mul_f32 v[234:235], v[234:235], v[242:243]
	v_pk_mul_f32 v[128:129], v[128:129], v[228:229]
	v_pk_mul_f32 v[130:131], v[130:131], v[230:231]
	v_pk_mul_f32 v[124:125], v[124:125], v[232:233]
	v_pk_mul_f32 v[126:127], v[126:127], v[234:235]
	s_waitcnt vmcnt(16)
	v_cvt_f32_ubyte0_e32 v228, v134
	v_cvt_f32_ubyte1_e32 v229, v134
	v_cvt_f32_ubyte2_e32 v230, v134
	v_cvt_f32_ubyte3_e32 v231, v134
	v_cvt_f32_ubyte0_e32 v232, v135
	v_cvt_f32_ubyte1_e32 v233, v135
	v_cvt_f32_ubyte2_e32 v234, v135
	v_cvt_f32_ubyte3_e32 v235, v135
	v_max_f32_e32 v228, 0x3985b185, v228
	v_max_f32_e32 v229, 0x3985b185, v229
	v_max_f32_e32 v230, 0x3985b185, v230
	v_max_f32_e32 v231, 0x3985b185, v231
	v_max_f32_e32 v232, 0x3985b185, v232
	v_max_f32_e32 v233, 0x3985b185, v233
	v_max_f32_e32 v234, 0x3985b185, v234
	v_max_f32_e32 v235, 0x3985b185, v235
	v_rcp_f32_e32 v228, v228
	v_rcp_f32_e32 v229, v229
	v_rcp_f32_e32 v230, v230
	v_rcp_f32_e32 v231, v231
	v_rcp_f32_e32 v232, v232
	v_rcp_f32_e32 v233, v233
	v_rcp_f32_e32 v234, v234
	v_rcp_f32_e32 v235, v235
	v_cvt_f32_ubyte0_e32 v236, v138
	v_cvt_f32_ubyte1_e32 v237, v138
	v_cvt_f32_ubyte2_e32 v238, v138
	v_cvt_f32_ubyte3_e32 v239, v138
	v_cvt_f32_ubyte0_e32 v240, v139
	v_cvt_f32_ubyte1_e32 v241, v139
	v_cvt_f32_ubyte2_e32 v242, v139
	v_cvt_f32_ubyte3_e32 v243, v139
	v_pk_mul_f32 v[228:229], v[228:229], v[236:237]
	v_pk_mul_f32 v[230:231], v[230:231], v[238:239]
	v_pk_mul_f32 v[232:233], v[232:233], v[240:241]
	v_pk_mul_f32 v[234:235], v[234:235], v[242:243]
	v_pk_mul_f32 v[112:113], v[112:113], v[228:229]
	v_pk_mul_f32 v[114:115], v[114:115], v[230:231]
	v_pk_mul_f32 v[108:109], v[108:109], v[232:233]
	v_pk_mul_f32 v[110:111], v[110:111], v[234:235]
	s_waitcnt vmcnt(14)
	v_cvt_f32_ubyte0_e32 v228, v174
	v_cvt_f32_ubyte1_e32 v229, v174
	v_cvt_f32_ubyte2_e32 v230, v174
	v_cvt_f32_ubyte3_e32 v231, v174
	v_cvt_f32_ubyte0_e32 v232, v175
	v_cvt_f32_ubyte1_e32 v233, v175
	v_cvt_f32_ubyte2_e32 v234, v175
	v_cvt_f32_ubyte3_e32 v235, v175
	v_max_f32_e32 v228, 0x3985b185, v228
	v_max_f32_e32 v229, 0x3985b185, v229
	v_max_f32_e32 v230, 0x3985b185, v230
	v_max_f32_e32 v231, 0x3985b185, v231
	v_max_f32_e32 v232, 0x3985b185, v232
	v_max_f32_e32 v233, 0x3985b185, v233
	v_max_f32_e32 v234, 0x3985b185, v234
	v_max_f32_e32 v235, 0x3985b185, v235
	v_rcp_f32_e32 v228, v228
	v_rcp_f32_e32 v229, v229
	v_rcp_f32_e32 v230, v230
	v_rcp_f32_e32 v231, v231
	v_rcp_f32_e32 v232, v232
	v_rcp_f32_e32 v233, v233
	v_rcp_f32_e32 v234, v234
	v_rcp_f32_e32 v235, v235
	v_cvt_f32_ubyte0_e32 v236, v178
	v_cvt_f32_ubyte1_e32 v237, v178
	v_cvt_f32_ubyte2_e32 v238, v178
	v_cvt_f32_ubyte3_e32 v239, v178
	v_cvt_f32_ubyte0_e32 v240, v179
	v_cvt_f32_ubyte1_e32 v241, v179
	v_cvt_f32_ubyte2_e32 v242, v179
	v_cvt_f32_ubyte3_e32 v243, v179
	v_pk_mul_f32 v[228:229], v[228:229], v[236:237]
	v_pk_mul_f32 v[230:231], v[230:231], v[238:239]
	v_pk_mul_f32 v[232:233], v[232:233], v[240:241]
	v_pk_mul_f32 v[234:235], v[234:235], v[242:243]
	v_pk_mul_f32 v[96:97], v[96:97], v[228:229]
	v_pk_mul_f32 v[98:99], v[98:99], v[230:231]
	v_pk_mul_f32 v[92:93], v[92:93], v[232:233]
	v_pk_mul_f32 v[94:95], v[94:95], v[234:235]
	s_waitcnt vmcnt(12)
	v_cvt_f32_ubyte0_e32 v228, v176
	v_cvt_f32_ubyte1_e32 v229, v176
	v_cvt_f32_ubyte2_e32 v230, v176
	v_cvt_f32_ubyte3_e32 v231, v176
	v_cvt_f32_ubyte0_e32 v232, v177
	v_cvt_f32_ubyte1_e32 v233, v177
	v_cvt_f32_ubyte2_e32 v234, v177
	v_cvt_f32_ubyte3_e32 v235, v177
	v_max_f32_e32 v228, 0x3985b185, v228
	v_max_f32_e32 v229, 0x3985b185, v229
	v_max_f32_e32 v230, 0x3985b185, v230
	v_max_f32_e32 v231, 0x3985b185, v231
	v_max_f32_e32 v232, 0x3985b185, v232
	v_max_f32_e32 v233, 0x3985b185, v233
	v_max_f32_e32 v234, 0x3985b185, v234
	v_max_f32_e32 v235, 0x3985b185, v235
	v_rcp_f32_e32 v228, v228
	v_rcp_f32_e32 v229, v229
	v_rcp_f32_e32 v230, v230
	v_rcp_f32_e32 v231, v231
	v_rcp_f32_e32 v232, v232
	v_rcp_f32_e32 v233, v233
	v_rcp_f32_e32 v234, v234
	v_rcp_f32_e32 v235, v235
	v_cvt_f32_ubyte0_e32 v236, v180
	v_cvt_f32_ubyte1_e32 v237, v180
	v_cvt_f32_ubyte2_e32 v238, v180
	v_cvt_f32_ubyte3_e32 v239, v180
	v_cvt_f32_ubyte0_e32 v240, v181
	v_cvt_f32_ubyte1_e32 v241, v181
	v_cvt_f32_ubyte2_e32 v242, v181
	v_cvt_f32_ubyte3_e32 v243, v181
	v_pk_mul_f32 v[228:229], v[228:229], v[236:237]
	v_pk_mul_f32 v[230:231], v[230:231], v[238:239]
	v_pk_mul_f32 v[232:233], v[232:233], v[240:241]
	v_pk_mul_f32 v[234:235], v[234:235], v[242:243]
	v_pk_mul_f32 v[80:81], v[80:81], v[228:229]
	v_pk_mul_f32 v[82:83], v[82:83], v[230:231]
	v_pk_mul_f32 v[76:77], v[76:77], v[232:233]
	v_pk_mul_f32 v[78:79], v[78:79], v[234:235]
	s_waitcnt vmcnt(10)
; __device__ __forceinline__ u32x4 pack8(const f32x4 a, const f32x4 b) { u32x4 w; w.x = cvt_pk_bf16(a[0], a[1]); w.y = cvt_pk_bf16(a[2], a[3]); w.z = cvt_pk_bf16(b[0], b[1]); w.w = cvt_pk_bf16(b[2], b[3]); return w; }
;     __device__ __forceinline__ void operator()(f32x4 (&acc)[2][2][4][2], const Unit& u, int wr, int wc, int fr, int fq) const {
;     ...
;                 for (int bj = 0; bj < 2; ++bj) { const u32x2 a2 = ga[c & 1][m2][bj], b2 = gb[c & 1][m2][bj]; const float q = 1.0f / 255.0f;
;                     const f32x4 sa0 = {(float)((a2.x >> 0) & 0xffu), (float)((a2.x >> 8) & 0xffu), (float)((a2.x >> 16) & 0xffu), (float)((a2.x >> 24) & 0xffu)};
;                     const f32x4 sa1 = {(float)((a2.y >> 0) & 0xffu), (float)((a2.y >> 8) & 0xffu), (float)((a2.y >> 16) & 0xffu), (float)((a2.y >> 24) & 0xffu)};
;                     f32x4 sb0 = {(float)((b2.x >> 0) & 0xffu), (float)((b2.x >> 8) & 0xffu), (float)((b2.x >> 16) & 0xffu), (float)((b2.x >> 24) & 0xffu)};
;                     f32x4 sb1 = {(float)((b2.y >> 0) & 0xffu), (float)((b2.y >> 8) & 0xffu), (float)((b2.y >> 16) & 0xffu), (float)((b2.y >> 24) & 0xffu)};
; #pragma unroll
;                     for (int e = 0; e < 4; ++e) { sb0[e] = fmaxf(sb0[e], 2.55e-4f); sb1[e] = fmaxf(sb1[e], 2.55e-4f); }
;                     if (second) *(u32x4*)(MERGED + (size_t)(row0 + ai * HALF + m * 16) * DM + col0 + bj * HALF) = pack8(acc[ai][bj][m][0] * (sb0 * q), acc[ai][bj][m][1] * (sb1 * q));
;                     if (!second) { f32x4 r0, r1;
; #pragma unroll
;                         for (int e = 0; e < 4; ++e) { r0[e] = sa0[e] * __builtin_amdgcn_rcpf(sb0[e]); r1[e] = sa1[e] * __builtin_amdgcn_rcpf(sb1[e]); }
;                         acc[ai][bj][m][0] = acc[ai][bj][m][0] * r0; acc[ai][bj][m][1] = acc[ai][bj][m][1] * r1; }
	v_cvt_f32_ubyte0_e32 v228, v182
	v_cvt_f32_ubyte1_e32 v229, v182
	v_cvt_f32_ubyte2_e32 v230, v182
	v_cvt_f32_ubyte3_e32 v231, v182
	v_cvt_f32_ubyte0_e32 v232, v183
	v_cvt_f32_ubyte1_e32 v233, v183
	v_cvt_f32_ubyte2_e32 v234, v183
	v_cvt_f32_ubyte3_e32 v235, v183
	v_max_f32_e32 v228, 0x3985b185, v228
	v_max_f32_e32 v229, 0x3985b185, v229
	v_max_f32_e32 v230, 0x3985b185, v230
	v_max_f32_e32 v231, 0x3985b185, v231
	v_max_f32_e32 v232, 0x3985b185, v232
	v_max_f32_e32 v233, 0x3985b185, v233
	v_max_f32_e32 v234, 0x3985b185, v234
	v_max_f32_e32 v235, 0x3985b185, v235
	v_rcp_f32_e32 v228, v228
	v_rcp_f32_e32 v229, v229
	v_rcp_f32_e32 v230, v230
	v_rcp_f32_e32 v231, v231
	v_rcp_f32_e32 v232, v232
	v_rcp_f32_e32 v233, v233
	v_rcp_f32_e32 v234, v234
	v_rcp_f32_e32 v235, v235
	v_cvt_f32_ubyte0_e32 v236, v186
	v_cvt_f32_ubyte1_e32 v237, v186
	v_cvt_f32_ubyte2_e32 v238, v186
	v_cvt_f32_ubyte3_e32 v239, v186
	v_cvt_f32_ubyte0_e32 v240, v187
	v_cvt_f32_ubyte1_e32 v241, v187
	v_cvt_f32_ubyte2_e32 v242, v187
	v_cvt_f32_ubyte3_e32 v243, v187
	v_pk_mul_f32 v[228:229], v[228:229], v[236:237]
	v_pk_mul_f32 v[230:231], v[230:231], v[238:239]
	v_pk_mul_f32 v[232:233], v[232:233], v[240:241]
	v_pk_mul_f32 v[234:235], v[234:235], v[242:243]
	v_pk_mul_f32 v[64:65], v[64:65], v[228:229]
	v_pk_mul_f32 v[66:67], v[66:67], v[230:231]
	v_pk_mul_f32 v[60:61], v[60:61], v[232:233]
	v_pk_mul_f32 v[62:63], v[62:63], v[234:235]
	s_waitcnt vmcnt(8)
	v_cvt_f32_ubyte0_e32 v228, v184
	v_cvt_f32_ubyte1_e32 v229, v184
	v_cvt_f32_ubyte2_e32 v230, v184
	v_cvt_f32_ubyte3_e32 v231, v184
	v_cvt_f32_ubyte0_e32 v232, v185
	v_cvt_f32_ubyte1_e32 v233, v185
	v_cvt_f32_ubyte2_e32 v234, v185
	v_cvt_f32_ubyte3_e32 v235, v185
	v_max_f32_e32 v228, 0x3985b185, v228
	v_max_f32_e32 v229, 0x3985b185, v229
	v_max_f32_e32 v230, 0x3985b185, v230
	v_max_f32_e32 v231, 0x3985b185, v231
	v_max_f32_e32 v232, 0x3985b185, v232
	v_max_f32_e32 v233, 0x3985b185, v233
	v_max_f32_e32 v234, 0x3985b185, v234
	v_max_f32_e32 v235, 0x3985b185, v235
	v_rcp_f32_e32 v228, v228
	v_rcp_f32_e32 v229, v229
	v_rcp_f32_e32 v230, v230
	v_rcp_f32_e32 v231, v231
	v_rcp_f32_e32 v232, v232
	v_rcp_f32_e32 v233, v233
	v_rcp_f32_e32 v234, v234
	v_rcp_f32_e32 v235, v235
	v_cvt_f32_ubyte0_e32 v236, v188
	v_cvt_f32_ubyte1_e32 v237, v188
	v_cvt_f32_ubyte2_e32 v238, v188
	v_cvt_f32_ubyte3_e32 v239, v188
	v_cvt_f32_ubyte0_e32 v240, v189
	v_cvt_f32_ubyte1_e32 v241, v189
	v_cvt_f32_ubyte2_e32 v242, v189
	v_cvt_f32_ubyte3_e32 v243, v189
	v_pk_mul_f32 v[228:229], v[228:229], v[236:237]
	v_pk_mul_f32 v[230:231], v[230:231], v[238:239]
	v_pk_mul_f32 v[232:233], v[232:233], v[240:241]
	v_pk_mul_f32 v[234:235], v[234:235], v[242:243]
	v_pk_mul_f32 v[48:49], v[48:49], v[228:229]
	v_pk_mul_f32 v[50:51], v[50:51], v[230:231]
	v_pk_mul_f32 v[44:45], v[44:45], v[232:233]
	v_pk_mul_f32 v[46:47], v[46:47], v[234:235]
	s_waitcnt vmcnt(6)
	v_cvt_f32_ubyte0_e32 v228, v190
	v_cvt_f32_ubyte1_e32 v229, v190
	v_cvt_f32_ubyte2_e32 v230, v190
	v_cvt_f32_ubyte3_e32 v231, v190
	v_cvt_f32_ubyte0_e32 v232, v191
	v_cvt_f32_ubyte1_e32 v233, v191
	v_cvt_f32_ubyte2_e32 v234, v191
	v_cvt_f32_ubyte3_e32 v235, v191
	v_max_f32_e32 v228, 0x3985b185, v228
	v_max_f32_e32 v229, 0x3985b185, v229
	v_max_f32_e32 v230, 0x3985b185, v230
	v_max_f32_e32 v231, 0x3985b185, v231
	v_max_f32_e32 v232, 0x3985b185, v232
	v_max_f32_e32 v233, 0x3985b185, v233
	v_max_f32_e32 v234, 0x3985b185, v234
	v_max_f32_e32 v235, 0x3985b185, v235
	v_rcp_f32_e32 v228, v228
	v_rcp_f32_e32 v229, v229
	v_rcp_f32_e32 v230, v230
	v_rcp_f32_e32 v231, v231
	v_rcp_f32_e32 v232, v232
	v_rcp_f32_e32 v233, v233
	v_rcp_f32_e32 v234, v234
	v_rcp_f32_e32 v235, v235
	v_cvt_f32_ubyte0_e32 v236, v194
	v_cvt_f32_ubyte1_e32 v237, v194
	v_cvt_f32_ubyte2_e32 v238, v194
	v_cvt_f32_ubyte3_e32 v239, v194
	v_cvt_f32_ubyte0_e32 v240, v195
	v_cvt_f32_ubyte1_e32 v241, v195
	v_cvt_f32_ubyte2_e32 v242, v195
	v_cvt_f32_ubyte3_e32 v243, v195
	v_pk_mul_f32 v[228:229], v[228:229], v[236:237]
	v_pk_mul_f32 v[230:231], v[230:231], v[238:239]
	v_pk_mul_f32 v[232:233], v[232:233], v[240:241]
	v_pk_mul_f32 v[234:235], v[234:235], v[242:243]
	v_pk_mul_f32 v[32:33], v[32:33], v[228:229]
	v_pk_mul_f32 v[34:35], v[34:35], v[230:231]
	v_pk_mul_f32 v[28:29], v[28:29], v[232:233]
	v_pk_mul_f32 v[30:31], v[30:31], v[234:235]
	s_waitcnt vmcnt(4)
	v_cvt_f32_ubyte0_e32 v228, v192
	v_cvt_f32_ubyte1_e32 v229, v192
	v_cvt_f32_ubyte2_e32 v230, v192
	v_cvt_f32_ubyte3_e32 v231, v192
	v_cvt_f32_ubyte0_e32 v232, v193
	v_cvt_f32_ubyte1_e32 v233, v193
	v_cvt_f32_ubyte2_e32 v234, v193
	v_cvt_f32_ubyte3_e32 v235, v193
	v_max_f32_e32 v228, 0x3985b185, v228
	v_max_f32_e32 v229, 0x3985b185, v229
	v_max_f32_e32 v230, 0x3985b185, v230
	v_max_f32_e32 v231, 0x3985b185, v231
	v_max_f32_e32 v232, 0x3985b185, v232
	v_max_f32_e32 v233, 0x3985b185, v233
	v_max_f32_e32 v234, 0x3985b185, v234
	v_max_f32_e32 v235, 0x3985b185, v235
	v_rcp_f32_e32 v228, v228
	v_rcp_f32_e32 v229, v229
	v_rcp_f32_e32 v230, v230
	v_rcp_f32_e32 v231, v231
	v_rcp_f32_e32 v232, v232
	v_rcp_f32_e32 v233, v233
	v_rcp_f32_e32 v234, v234
	v_rcp_f32_e32 v235, v235
	v_cvt_f32_ubyte0_e32 v236, v196
	v_cvt_f32_ubyte1_e32 v237, v196
	v_cvt_f32_ubyte2_e32 v238, v196
	v_cvt_f32_ubyte3_e32 v239, v196
	v_cvt_f32_ubyte0_e32 v240, v197
	v_cvt_f32_ubyte1_e32 v241, v197
	v_cvt_f32_ubyte2_e32 v242, v197
	v_cvt_f32_ubyte3_e32 v243, v197
	v_pk_mul_f32 v[228:229], v[228:229], v[236:237]
	v_pk_mul_f32 v[230:231], v[230:231], v[238:239]
	v_pk_mul_f32 v[232:233], v[232:233], v[240:241]
	v_pk_mul_f32 v[234:235], v[234:235], v[242:243]
	v_pk_mul_f32 v[24:25], v[24:25], v[228:229]
	v_pk_mul_f32 v[26:27], v[26:27], v[230:231]
	v_pk_mul_f32 v[20:21], v[20:21], v[232:233]
	v_pk_mul_f32 v[22:23], v[22:23], v[234:235]
	s_waitcnt vmcnt(2)
; __device__ __forceinline__ u32x4 pack8(const f32x4 a, const f32x4 b) { u32x4 w; w.x = cvt_pk_bf16(a[0], a[1]); w.y = cvt_pk_bf16(a[2], a[3]); w.z = cvt_pk_bf16(b[0], b[1]); w.w = cvt_pk_bf16(b[2], b[3]); return w; }
;     __device__ __forceinline__ void operator()(f32x4 (&acc)[2][2][4][2], const Unit& u, int wr, int wc, int fr, int fq) const {
;     ...
;                 for (int bj = 0; bj < 2; ++bj) { const u32x2 a2 = ga[c & 1][m2][bj], b2 = gb[c & 1][m2][bj]; const float q = 1.0f / 255.0f;
;                     const f32x4 sa0 = {(float)((a2.x >> 0) & 0xffu), (float)((a2.x >> 8) & 0xffu), (float)((a2.x >> 16) & 0xffu), (float)((a2.x >> 24) & 0xffu)};
;                     const f32x4 sa1 = {(float)((a2.y >> 0) & 0xffu), (float)((a2.y >> 8) & 0xffu), (float)((a2.y >> 16) & 0xffu), (float)((a2.y >> 24) & 0xffu)};
;                     f32x4 sb0 = {(float)((b2.x >> 0) & 0xffu), (float)((b2.x >> 8) & 0xffu), (float)((b2.x >> 16) & 0xffu), (float)((b2.x >> 24) & 0xffu)};
;                     f32x4 sb1 = {(float)((b2.y >> 0) & 0xffu), (float)((b2.y >> 8) & 0xffu), (float)((b2.y >> 16) & 0xffu), (float)((b2.y >> 24) & 0xffu)};
; #pragma unroll
;                     for (int e = 0; e < 4; ++e) { sb0[e] = fmaxf(sb0[e], 2.55e-4f); sb1[e] = fmaxf(sb1[e], 2.55e-4f); }
;                     if (second) *(u32x4*)(MERGED + (size_t)(row0 + ai * HALF + m * 16) * DM + col0 + bj * HALF) = pack8(acc[ai][bj][m][0] * (sb0 * q), acc[ai][bj][m][1] * (sb1 * q));
;                     if (!second) { f32x4 r0, r1;
; #pragma unroll
;                         for (int e = 0; e < 4; ++e) { r0[e] = sa0[e] * __builtin_amdgcn_rcpf(sb0[e]); r1[e] = sa1[e] * __builtin_amdgcn_rcpf(sb1[e]); }
;                         acc[ai][bj][m][0] = acc[ai][bj][m][0] * r0; acc[ai][bj][m][1] = acc[ai][bj][m][1] * r1; }
;                     else { acc[ai][bj][m][0] = (f32x4){0.f, 0.f, 0.f, 0.f}; acc[ai][bj][m][1] = (f32x4){0.f, 0.f, 0.f, 0.f}; } }
	v_cvt_f32_ubyte0_e32 v228, v204
	v_cvt_f32_ubyte1_e32 v229, v204
	v_cvt_f32_ubyte2_e32 v230, v204
	v_cvt_f32_ubyte3_e32 v231, v204
	v_cvt_f32_ubyte0_e32 v232, v205
	v_cvt_f32_ubyte1_e32 v233, v205
	v_cvt_f32_ubyte2_e32 v234, v205
	v_cvt_f32_ubyte3_e32 v235, v205
	v_max_f32_e32 v228, 0x3985b185, v228
	v_max_f32_e32 v229, 0x3985b185, v229
	v_max_f32_e32 v230, 0x3985b185, v230
	v_max_f32_e32 v231, 0x3985b185, v231
	v_max_f32_e32 v232, 0x3985b185, v232
	v_max_f32_e32 v233, 0x3985b185, v233
	v_max_f32_e32 v234, 0x3985b185, v234
	v_max_f32_e32 v235, 0x3985b185, v235
	v_rcp_f32_e32 v228, v228
	v_rcp_f32_e32 v229, v229
	v_rcp_f32_e32 v230, v230
	v_rcp_f32_e32 v231, v231
	v_rcp_f32_e32 v232, v232
	v_rcp_f32_e32 v233, v233
	v_rcp_f32_e32 v234, v234
	v_rcp_f32_e32 v235, v235
	v_cvt_f32_ubyte0_e32 v236, v208
	v_cvt_f32_ubyte1_e32 v237, v208
	v_cvt_f32_ubyte2_e32 v238, v208
	v_cvt_f32_ubyte3_e32 v239, v208
	v_cvt_f32_ubyte0_e32 v240, v209
	v_cvt_f32_ubyte1_e32 v241, v209
	v_cvt_f32_ubyte2_e32 v242, v209
	v_cvt_f32_ubyte3_e32 v243, v209
	v_pk_mul_f32 v[228:229], v[228:229], v[236:237]
	v_pk_mul_f32 v[230:231], v[230:231], v[238:239]
	v_pk_mul_f32 v[232:233], v[232:233], v[240:241]
	v_pk_mul_f32 v[234:235], v[234:235], v[242:243]
	v_pk_mul_f32 v[16:17], v[16:17], v[228:229]
	v_pk_mul_f32 v[18:19], v[18:19], v[230:231]
	v_pk_mul_f32 v[12:13], v[12:13], v[232:233]
	v_pk_mul_f32 v[14:15], v[14:15], v[234:235]
	s_waitcnt vmcnt(0)
	v_cvt_f32_ubyte0_e32 v228, v206
	v_cvt_f32_ubyte1_e32 v229, v206
	v_cvt_f32_ubyte2_e32 v230, v206
	v_cvt_f32_ubyte3_e32 v231, v206
	v_cvt_f32_ubyte0_e32 v232, v207
	v_cvt_f32_ubyte1_e32 v233, v207
	v_cvt_f32_ubyte2_e32 v234, v207
	v_cvt_f32_ubyte3_e32 v235, v207
	v_max_f32_e32 v228, 0x3985b185, v228
	v_max_f32_e32 v229, 0x3985b185, v229
	v_max_f32_e32 v230, 0x3985b185, v230
	v_max_f32_e32 v231, 0x3985b185, v231
	v_max_f32_e32 v232, 0x3985b185, v232
	v_max_f32_e32 v233, 0x3985b185, v233
	v_max_f32_e32 v234, 0x3985b185, v234
	v_max_f32_e32 v235, 0x3985b185, v235
	v_rcp_f32_e32 v228, v228
	v_rcp_f32_e32 v229, v229
	v_rcp_f32_e32 v230, v230
	v_rcp_f32_e32 v231, v231
	v_rcp_f32_e32 v232, v232
	v_rcp_f32_e32 v233, v233
	v_rcp_f32_e32 v234, v234
	v_rcp_f32_e32 v235, v235
	v_cvt_f32_ubyte0_e32 v236, v210
	v_cvt_f32_ubyte1_e32 v237, v210
	v_cvt_f32_ubyte2_e32 v238, v210
	v_cvt_f32_ubyte3_e32 v239, v210
	v_cvt_f32_ubyte0_e32 v240, v211
	v_cvt_f32_ubyte1_e32 v241, v211
	v_cvt_f32_ubyte2_e32 v242, v211
	v_cvt_f32_ubyte3_e32 v243, v211
	v_pk_mul_f32 v[228:229], v[228:229], v[236:237]
	v_pk_mul_f32 v[230:231], v[230:231], v[238:239]
	v_pk_mul_f32 v[232:233], v[232:233], v[240:241]
	v_pk_mul_f32 v[234:235], v[234:235], v[242:243]
	v_pk_mul_f32 v[8:9], v[8:9], v[228:229]
	v_pk_mul_f32 v[10:11], v[10:11], v[230:231]
	v_pk_mul_f32 v[4:5], v[4:5], v[232:233]
	v_pk_mul_f32 v[6:7], v[6:7], v[234:235]
	s_branch .Lmg_end
.Lmg_second:
	s_lshl_b32 s1, s4, 8
	s_lshl_b32 s5, s0, 8
	s_add_i32 s1, s1, 0xffffc000
	s_add_i32 s5, s5, 0xfffffc00
	v_add_u32_e32 v253, s1, v200
	v_or_b32_e32 v252, s5, v202
	v_lshl_add_u32 v252, v253, 10, v252
	v_lshlrev_b32_e32 v253, 1, v252
	global_load_dwordx2 v[36:37], v252, s[10:11]
	global_load_dwordx2 v[38:39], v252, s[10:11] offset:128
	v_add_u32_e32 v252, 0x4000, v252
	global_load_dwordx2 v[40:41], v252, s[10:11]
	global_load_dwordx2 v[42:43], v252, s[10:11] offset:128
	v_add_u32_e32 v252, 0x4000, v252
	global_load_dwordx2 v[68:69], v252, s[10:11]
	global_load_dwordx2 v[70:71], v252, s[10:11] offset:128
	v_add_u32_e32 v252, 0x4000, v252
	global_load_dwordx2 v[72:73], v252, s[10:11]
	global_load_dwordx2 v[74:75], v252, s[10:11] offset:128
	v_add_u32_e32 v252, 0x14000, v252
	global_load_dwordx2 v[100:101], v252, s[10:11]
	global_load_dwordx2 v[102:103], v252, s[10:11] offset:128
	v_add_u32_e32 v252, 0x4000, v252
	global_load_dwordx2 v[104:105], v252, s[10:11]
	global_load_dwordx2 v[106:107], v252, s[10:11] offset:128
	v_add_u32_e32 v252, 0x4000, v252
	global_load_dwordx2 v[132:133], v252, s[10:11]
	global_load_dwordx2 v[134:135], v252, s[10:11] offset:128
	v_add_u32_e32 v252, 0x4000, v252
	global_load_dwordx2 v[136:137], v252, s[10:11]
	global_load_dwordx2 v[138:139], v252, s[10:11] offset:128
	s_waitcnt vmcnt(15)
	v_cvt_f32_ubyte0_e32 v228, v36
	v_cvt_f32_ubyte1_e32 v229, v36
	v_cvt_f32_ubyte2_e32 v230, v36
	v_cvt_f32_ubyte3_e32 v231, v36
	v_cvt_f32_ubyte0_e32 v232, v37
	v_cvt_f32_ubyte1_e32 v233, v37
	v_cvt_f32_ubyte2_e32 v234, v37
	v_cvt_f32_ubyte3_e32 v235, v37
	v_max_f32_e32 v228, 0x3985b185, v228
	v_max_f32_e32 v229, 0x3985b185, v229
	v_max_f32_e32 v230, 0x3985b185, v230
	v_max_f32_e32 v231, 0x3985b185, v231
	v_max_f32_e32 v232, 0x3985b185, v232
	v_max_f32_e32 v233, 0x3985b185, v233
	v_max_f32_e32 v234, 0x3985b185, v234
	v_max_f32_e32 v235, 0x3985b185, v235
	v_pk_mul_f32 v[228:229], v[228:229], s[54:55] op_sel_hi:[1,0]
	v_pk_mul_f32 v[230:231], v[230:231], s[54:55] op_sel_hi:[1,0]
	v_pk_mul_f32 v[232:233], v[232:233], s[54:55] op_sel_hi:[1,0]
	v_pk_mul_f32 v[234:235], v[234:235], s[54:55] op_sel_hi:[1,0]
	v_pk_mul_f32 v[228:229], v[56:57], v[228:229]
	v_pk_mul_f32 v[230:231], v[58:59], v[230:231]
	v_pk_mul_f32 v[232:233], v[52:53], v[232:233]
	v_pk_mul_f32 v[234:235], v[54:55], v[234:235]
	v_cvt_pk_bf16_f32 v244, v228, v229
	v_cvt_pk_bf16_f32 v245, v230, v231
	v_cvt_pk_bf16_f32 v246, v232, v233
	v_cvt_pk_bf16_f32 v247, v234, v235
	global_store_dwordx4 v253, v[244:247], s[12:13]
	s_waitcnt vmcnt(15)
; __device__ __forceinline__ u32x4 pack8(const f32x4 a, const f32x4 b) { u32x4 w; w.x = cvt_pk_bf16(a[0], a[1]); w.y = cvt_pk_bf16(a[2], a[3]); w.z = cvt_pk_bf16(b[0], b[1]); w.w = cvt_pk_bf16(b[2], b[3]); return w; }
;     __device__ __forceinline__ void operator()(f32x4 (&acc)[2][2][4][2], const Unit& u, int wr, int wc, int fr, int fq) const {
;     ...
;                 for (int bj = 0; bj < 2; ++bj) { const u32x2 a2 = ga[c & 1][m2][bj], b2 = gb[c & 1][m2][bj]; const float q = 1.0f / 255.0f;
;                     const f32x4 sa0 = {(float)((a2.x >> 0) & 0xffu), (float)((a2.x >> 8) & 0xffu), (float)((a2.x >> 16) & 0xffu), (float)((a2.x >> 24) & 0xffu)};
;                     const f32x4 sa1 = {(float)((a2.y >> 0) & 0xffu), (float)((a2.y >> 8) & 0xffu), (float)((a2.y >> 16) & 0xffu), (float)((a2.y >> 24) & 0xffu)};
;                     f32x4 sb0 = {(float)((b2.x >> 0) & 0xffu), (float)((b2.x >> 8) & 0xffu), (float)((b2.x >> 16) & 0xffu), (float)((b2.x >> 24) & 0xffu)};
;                     f32x4 sb1 = {(float)((b2.y >> 0) & 0xffu), (float)((b2.y >> 8) & 0xffu), (float)((b2.y >> 16) & 0xffu), (float)((b2.y >> 24) & 0xffu)};
; #pragma unroll
;                     for (int e = 0; e < 4; ++e) { sb0[e] = fmaxf(sb0[e], 2.55e-4f); sb1[e] = fmaxf(sb1[e], 2.55e-4f); }
;                     if (second) *(u32x4*)(MERGED + (size_t)(row0 + ai * HALF + m * 16) * DM + col0 + bj * HALF) = pack8(acc[ai][bj][m][0] * (sb0 * q), acc[ai][bj][m][1] * (sb1 * q));
	v_cvt_f32_ubyte0_e32 v228, v38
	v_cvt_f32_ubyte1_e32 v229, v38
	v_cvt_f32_ubyte2_e32 v230, v38
	v_cvt_f32_ubyte3_e32 v231, v38
	v_cvt_f32_ubyte0_e32 v232, v39
	v_cvt_f32_ubyte1_e32 v233, v39
	v_cvt_f32_ubyte2_e32 v234, v39
	v_cvt_f32_ubyte3_e32 v235, v39
	v_max_f32_e32 v228, 0x3985b185, v228
	v_max_f32_e32 v229, 0x3985b185, v229
	v_max_f32_e32 v230, 0x3985b185, v230
	v_max_f32_e32 v231, 0x3985b185, v231
	v_max_f32_e32 v232, 0x3985b185, v232
	v_max_f32_e32 v233, 0x3985b185, v233
	v_max_f32_e32 v234, 0x3985b185, v234
	v_max_f32_e32 v235, 0x3985b185, v235
	v_pk_mul_f32 v[228:229], v[228:229], s[54:55] op_sel_hi:[1,0]
	v_pk_mul_f32 v[230:231], v[230:231], s[54:55] op_sel_hi:[1,0]
	v_pk_mul_f32 v[232:233], v[232:233], s[54:55] op_sel_hi:[1,0]
	v_pk_mul_f32 v[234:235], v[234:235], s[54:55] op_sel_hi:[1,0]
	v_pk_mul_f32 v[228:229], v[160:161], v[228:229]
	v_pk_mul_f32 v[230:231], v[162:163], v[230:231]
	v_pk_mul_f32 v[232:233], v[156:157], v[232:233]
	v_pk_mul_f32 v[234:235], v[158:159], v[234:235]
	v_cvt_pk_bf16_f32 v248, v228, v229
	v_cvt_pk_bf16_f32 v249, v230, v231
	v_cvt_pk_bf16_f32 v250, v232, v233
	v_cvt_pk_bf16_f32 v251, v234, v235
	global_store_dwordx4 v253, v[248:251], s[12:13] offset:256
	v_add_u32_e32 v253, 0x8000, v253
	s_waitcnt vmcnt(15)
	v_cvt_f32_ubyte0_e32 v228, v40
	v_cvt_f32_ubyte1_e32 v229, v40
	v_cvt_f32_ubyte2_e32 v230, v40
	v_cvt_f32_ubyte3_e32 v231, v40
	v_cvt_f32_ubyte0_e32 v232, v41
	v_cvt_f32_ubyte1_e32 v233, v41
	v_cvt_f32_ubyte2_e32 v234, v41
	v_cvt_f32_ubyte3_e32 v235, v41
	v_max_f32_e32 v228, 0x3985b185, v228
	v_max_f32_e32 v229, 0x3985b185, v229
	v_max_f32_e32 v230, 0x3985b185, v230
	v_max_f32_e32 v231, 0x3985b185, v231
	v_max_f32_e32 v232, 0x3985b185, v232
	v_max_f32_e32 v233, 0x3985b185, v233
	v_max_f32_e32 v234, 0x3985b185, v234
	v_max_f32_e32 v235, 0x3985b185, v235
	v_pk_mul_f32 v[228:229], v[228:229], s[54:55] op_sel_hi:[1,0]
	v_pk_mul_f32 v[230:231], v[230:231], s[54:55] op_sel_hi:[1,0]
	v_pk_mul_f32 v[232:233], v[232:233], s[54:55] op_sel_hi:[1,0]
	v_pk_mul_f32 v[234:235], v[234:235], s[54:55] op_sel_hi:[1,0]
	v_pk_mul_f32 v[228:229], v[88:89], v[228:229]
	v_pk_mul_f32 v[230:231], v[90:91], v[230:231]
	v_pk_mul_f32 v[232:233], v[84:85], v[232:233]
	v_pk_mul_f32 v[234:235], v[86:87], v[234:235]
	v_cvt_pk_bf16_f32 v244, v228, v229
	v_cvt_pk_bf16_f32 v245, v230, v231
	v_cvt_pk_bf16_f32 v246, v232, v233
	v_cvt_pk_bf16_f32 v247, v234, v235
	global_store_dwordx4 v253, v[244:247], s[12:13]
	s_waitcnt vmcnt(15)
	v_cvt_f32_ubyte0_e32 v228, v42
	v_cvt_f32_ubyte1_e32 v229, v42
	v_cvt_f32_ubyte2_e32 v230, v42
	v_cvt_f32_ubyte3_e32 v231, v42
	v_cvt_f32_ubyte0_e32 v232, v43
	v_cvt_f32_ubyte1_e32 v233, v43
	v_cvt_f32_ubyte2_e32 v234, v43
	v_cvt_f32_ubyte3_e32 v235, v43
	v_max_f32_e32 v228, 0x3985b185, v228
	v_max_f32_e32 v229, 0x3985b185, v229
	v_max_f32_e32 v230, 0x3985b185, v230
	v_max_f32_e32 v231, 0x3985b185, v231
	v_max_f32_e32 v232, 0x3985b185, v232
	v_max_f32_e32 v233, 0x3985b185, v233
	v_max_f32_e32 v234, 0x3985b185, v234
	v_max_f32_e32 v235, 0x3985b185, v235
	v_pk_mul_f32 v[228:229], v[228:229], s[54:55] op_sel_hi:[1,0]
	v_pk_mul_f32 v[230:231], v[230:231], s[54:55] op_sel_hi:[1,0]
	v_pk_mul_f32 v[232:233], v[232:233], s[54:55] op_sel_hi:[1,0]
	v_pk_mul_f32 v[234:235], v[234:235], s[54:55] op_sel_hi:[1,0]
	v_pk_mul_f32 v[228:229], v[152:153], v[228:229]
	v_pk_mul_f32 v[230:231], v[154:155], v[230:231]
	v_pk_mul_f32 v[232:233], v[148:149], v[232:233]
	v_pk_mul_f32 v[234:235], v[150:151], v[234:235]
	v_cvt_pk_bf16_f32 v248, v228, v229
	v_cvt_pk_bf16_f32 v249, v230, v231
	v_cvt_pk_bf16_f32 v250, v232, v233
	v_cvt_pk_bf16_f32 v251, v234, v235
	global_store_dwordx4 v253, v[248:251], s[12:13] offset:256
	v_add_u32_e32 v253, 0x8000, v253
	s_waitcnt vmcnt(15)
	v_cvt_f32_ubyte0_e32 v228, v68
	v_cvt_f32_ubyte1_e32 v229, v68
	v_cvt_f32_ubyte2_e32 v230, v68
	v_cvt_f32_ubyte3_e32 v231, v68
	v_cvt_f32_ubyte0_e32 v232, v69
	v_cvt_f32_ubyte1_e32 v233, v69
	v_cvt_f32_ubyte2_e32 v234, v69
	v_cvt_f32_ubyte3_e32 v235, v69
	v_max_f32_e32 v228, 0x3985b185, v228
	v_max_f32_e32 v229, 0x3985b185, v229
	v_max_f32_e32 v230, 0x3985b185, v230
	v_max_f32_e32 v231, 0x3985b185, v231
	v_max_f32_e32 v232, 0x3985b185, v232
	v_max_f32_e32 v233, 0x3985b185, v233
	v_max_f32_e32 v234, 0x3985b185, v234
	v_max_f32_e32 v235, 0x3985b185, v235
	v_pk_mul_f32 v[228:229], v[228:229], s[54:55] op_sel_hi:[1,0]
	v_pk_mul_f32 v[230:231], v[230:231], s[54:55] op_sel_hi:[1,0]
	v_pk_mul_f32 v[232:233], v[232:233], s[54:55] op_sel_hi:[1,0]
	v_pk_mul_f32 v[234:235], v[234:235], s[54:55] op_sel_hi:[1,0]
	v_pk_mul_f32 v[228:229], v[120:121], v[228:229]
	v_pk_mul_f32 v[230:231], v[122:123], v[230:231]
	v_pk_mul_f32 v[232:233], v[116:117], v[232:233]
	v_pk_mul_f32 v[234:235], v[118:119], v[234:235]
	v_cvt_pk_bf16_f32 v244, v228, v229
	v_cvt_pk_bf16_f32 v245, v230, v231
	v_cvt_pk_bf16_f32 v246, v232, v233
	v_cvt_pk_bf16_f32 v247, v234, v235
	global_store_dwordx4 v253, v[244:247], s[12:13]
	s_waitcnt vmcnt(15)
	v_cvt_f32_ubyte0_e32 v228, v70
	v_cvt_f32_ubyte1_e32 v229, v70
	v_cvt_f32_ubyte2_e32 v230, v70
	v_cvt_f32_ubyte3_e32 v231, v70
	v_cvt_f32_ubyte0_e32 v232, v71
	v_cvt_f32_ubyte1_e32 v233, v71
	v_cvt_f32_ubyte2_e32 v234, v71
	v_cvt_f32_ubyte3_e32 v235, v71
	v_max_f32_e32 v228, 0x3985b185, v228
	v_max_f32_e32 v229, 0x3985b185, v229
	v_max_f32_e32 v230, 0x3985b185, v230
	v_max_f32_e32 v231, 0x3985b185, v231
	v_max_f32_e32 v232, 0x3985b185, v232
	v_max_f32_e32 v233, 0x3985b185, v233
	v_max_f32_e32 v234, 0x3985b185, v234
	v_max_f32_e32 v235, 0x3985b185, v235
	v_pk_mul_f32 v[228:229], v[228:229], s[54:55] op_sel_hi:[1,0]
	v_pk_mul_f32 v[230:231], v[230:231], s[54:55] op_sel_hi:[1,0]
	v_pk_mul_f32 v[232:233], v[232:233], s[54:55] op_sel_hi:[1,0]
	v_pk_mul_f32 v[234:235], v[234:235], s[54:55] op_sel_hi:[1,0]
	v_pk_mul_f32 v[228:229], v[144:145], v[228:229]
	v_pk_mul_f32 v[230:231], v[146:147], v[230:231]
	v_pk_mul_f32 v[232:233], v[140:141], v[232:233]
	v_pk_mul_f32 v[234:235], v[142:143], v[234:235]
	v_cvt_pk_bf16_f32 v248, v228, v229
	v_cvt_pk_bf16_f32 v249, v230, v231
	v_cvt_pk_bf16_f32 v250, v232, v233
	v_cvt_pk_bf16_f32 v251, v234, v235
	global_store_dwordx4 v253, v[248:251], s[12:13] offset:256
	v_add_u32_e32 v253, 0x8000, v253
	s_waitcnt vmcnt(15)
; __device__ __forceinline__ u32x4 pack8(const f32x4 a, const f32x4 b) { u32x4 w; w.x = cvt_pk_bf16(a[0], a[1]); w.y = cvt_pk_bf16(a[2], a[3]); w.z = cvt_pk_bf16(b[0], b[1]); w.w = cvt_pk_bf16(b[2], b[3]); return w; }
;     __device__ __forceinline__ void operator()(f32x4 (&acc)[2][2][4][2], const Unit& u, int wr, int wc, int fr, int fq) const {
;     ...
;                 for (int bj = 0; bj < 2; ++bj) { const u32x2 a2 = ga[c & 1][m2][bj], b2 = gb[c & 1][m2][bj]; const float q = 1.0f / 255.0f;
;                     const f32x4 sa0 = {(float)((a2.x >> 0) & 0xffu), (float)((a2.x >> 8) & 0xffu), (float)((a2.x >> 16) & 0xffu), (float)((a2.x >> 24) & 0xffu)};
;                     const f32x4 sa1 = {(float)((a2.y >> 0) & 0xffu), (float)((a2.y >> 8) & 0xffu), (float)((a2.y >> 16) & 0xffu), (float)((a2.y >> 24) & 0xffu)};
;                     f32x4 sb0 = {(float)((b2.x >> 0) & 0xffu), (float)((b2.x >> 8) & 0xffu), (float)((b2.x >> 16) & 0xffu), (float)((b2.x >> 24) & 0xffu)};
;                     f32x4 sb1 = {(float)((b2.y >> 0) & 0xffu), (float)((b2.y >> 8) & 0xffu), (float)((b2.y >> 16) & 0xffu), (float)((b2.y >> 24) & 0xffu)};
; #pragma unroll
;                     for (int e = 0; e < 4; ++e) { sb0[e] = fmaxf(sb0[e], 2.55e-4f); sb1[e] = fmaxf(sb1[e], 2.55e-4f); }
;                     if (second) *(u32x4*)(MERGED + (size_t)(row0 + ai * HALF + m * 16) * DM + col0 + bj * HALF) = pack8(acc[ai][bj][m][0] * (sb0 * q), acc[ai][bj][m][1] * (sb1 * q));
	v_cvt_f32_ubyte0_e32 v228, v72
	v_cvt_f32_ubyte1_e32 v229, v72
	v_cvt_f32_ubyte2_e32 v230, v72
	v_cvt_f32_ubyte3_e32 v231, v72
	v_cvt_f32_ubyte0_e32 v232, v73
	v_cvt_f32_ubyte1_e32 v233, v73
	v_cvt_f32_ubyte2_e32 v234, v73
	v_cvt_f32_ubyte3_e32 v235, v73
	v_max_f32_e32 v228, 0x3985b185, v228
	v_max_f32_e32 v229, 0x3985b185, v229
	v_max_f32_e32 v230, 0x3985b185, v230
	v_max_f32_e32 v231, 0x3985b185, v231
	v_max_f32_e32 v232, 0x3985b185, v232
	v_max_f32_e32 v233, 0x3985b185, v233
	v_max_f32_e32 v234, 0x3985b185, v234
	v_max_f32_e32 v235, 0x3985b185, v235
	v_pk_mul_f32 v[228:229], v[228:229], s[54:55] op_sel_hi:[1,0]
	v_pk_mul_f32 v[230:231], v[230:231], s[54:55] op_sel_hi:[1,0]
	v_pk_mul_f32 v[232:233], v[232:233], s[54:55] op_sel_hi:[1,0]
	v_pk_mul_f32 v[234:235], v[234:235], s[54:55] op_sel_hi:[1,0]
	v_pk_mul_f32 v[228:229], v[128:129], v[228:229]
	v_pk_mul_f32 v[230:231], v[130:131], v[230:231]
	v_pk_mul_f32 v[232:233], v[124:125], v[232:233]
	v_pk_mul_f32 v[234:235], v[126:127], v[234:235]
	v_cvt_pk_bf16_f32 v244, v228, v229
	v_cvt_pk_bf16_f32 v245, v230, v231
	v_cvt_pk_bf16_f32 v246, v232, v233
	v_cvt_pk_bf16_f32 v247, v234, v235
	global_store_dwordx4 v253, v[244:247], s[12:13]
	s_waitcnt vmcnt(15)
	v_cvt_f32_ubyte0_e32 v228, v74
	v_cvt_f32_ubyte1_e32 v229, v74
	v_cvt_f32_ubyte2_e32 v230, v74
	v_cvt_f32_ubyte3_e32 v231, v74
	v_cvt_f32_ubyte0_e32 v232, v75
	v_cvt_f32_ubyte1_e32 v233, v75
	v_cvt_f32_ubyte2_e32 v234, v75
	v_cvt_f32_ubyte3_e32 v235, v75
	v_max_f32_e32 v228, 0x3985b185, v228
	v_max_f32_e32 v229, 0x3985b185, v229
	v_max_f32_e32 v230, 0x3985b185, v230
	v_max_f32_e32 v231, 0x3985b185, v231
	v_max_f32_e32 v232, 0x3985b185, v232
	v_max_f32_e32 v233, 0x3985b185, v233
	v_max_f32_e32 v234, 0x3985b185, v234
	v_max_f32_e32 v235, 0x3985b185, v235
	v_pk_mul_f32 v[228:229], v[228:229], s[54:55] op_sel_hi:[1,0]
	v_pk_mul_f32 v[230:231], v[230:231], s[54:55] op_sel_hi:[1,0]
	v_pk_mul_f32 v[232:233], v[232:233], s[54:55] op_sel_hi:[1,0]
	v_pk_mul_f32 v[234:235], v[234:235], s[54:55] op_sel_hi:[1,0]
	v_pk_mul_f32 v[228:229], v[112:113], v[228:229]
	v_pk_mul_f32 v[230:231], v[114:115], v[230:231]
	v_pk_mul_f32 v[232:233], v[108:109], v[232:233]
	v_pk_mul_f32 v[234:235], v[110:111], v[234:235]
	v_cvt_pk_bf16_f32 v248, v228, v229
	v_cvt_pk_bf16_f32 v249, v230, v231
	v_cvt_pk_bf16_f32 v250, v232, v233
	v_cvt_pk_bf16_f32 v251, v234, v235
	global_store_dwordx4 v253, v[248:251], s[12:13] offset:256
	v_add_u32_e32 v253, 0x28000, v253
	s_waitcnt vmcnt(15)
	v_cvt_f32_ubyte0_e32 v228, v100
	v_cvt_f32_ubyte1_e32 v229, v100
	v_cvt_f32_ubyte2_e32 v230, v100
	v_cvt_f32_ubyte3_e32 v231, v100
	v_cvt_f32_ubyte0_e32 v232, v101
	v_cvt_f32_ubyte1_e32 v233, v101
	v_cvt_f32_ubyte2_e32 v234, v101
	v_cvt_f32_ubyte3_e32 v235, v101
	v_max_f32_e32 v228, 0x3985b185, v228
	v_max_f32_e32 v229, 0x3985b185, v229
	v_max_f32_e32 v230, 0x3985b185, v230
	v_max_f32_e32 v231, 0x3985b185, v231
	v_max_f32_e32 v232, 0x3985b185, v232
	v_max_f32_e32 v233, 0x3985b185, v233
	v_max_f32_e32 v234, 0x3985b185, v234
	v_max_f32_e32 v235, 0x3985b185, v235
	v_pk_mul_f32 v[228:229], v[228:229], s[54:55] op_sel_hi:[1,0]
	v_pk_mul_f32 v[230:231], v[230:231], s[54:55] op_sel_hi:[1,0]
	v_pk_mul_f32 v[232:233], v[232:233], s[54:55] op_sel_hi:[1,0]
	v_pk_mul_f32 v[234:235], v[234:235], s[54:55] op_sel_hi:[1,0]
	v_pk_mul_f32 v[228:229], v[96:97], v[228:229]
	v_pk_mul_f32 v[230:231], v[98:99], v[230:231]
	v_pk_mul_f32 v[232:233], v[92:93], v[232:233]
	v_pk_mul_f32 v[234:235], v[94:95], v[234:235]
	v_cvt_pk_bf16_f32 v244, v228, v229
	v_cvt_pk_bf16_f32 v245, v230, v231
	v_cvt_pk_bf16_f32 v246, v232, v233
	v_cvt_pk_bf16_f32 v247, v234, v235
	global_store_dwordx4 v253, v[244:247], s[12:13]
	s_waitcnt vmcnt(15)
	v_cvt_f32_ubyte0_e32 v228, v102
	v_cvt_f32_ubyte1_e32 v229, v102
	v_cvt_f32_ubyte2_e32 v230, v102
	v_cvt_f32_ubyte3_e32 v231, v102
	v_cvt_f32_ubyte0_e32 v232, v103
	v_cvt_f32_ubyte1_e32 v233, v103
	v_cvt_f32_ubyte2_e32 v234, v103
	v_cvt_f32_ubyte3_e32 v235, v103
	v_max_f32_e32 v228, 0x3985b185, v228
	v_max_f32_e32 v229, 0x3985b185, v229
	v_max_f32_e32 v230, 0x3985b185, v230
	v_max_f32_e32 v231, 0x3985b185, v231
	v_max_f32_e32 v232, 0x3985b185, v232
	v_max_f32_e32 v233, 0x3985b185, v233
	v_max_f32_e32 v234, 0x3985b185, v234
	v_max_f32_e32 v235, 0x3985b185, v235
	v_pk_mul_f32 v[228:229], v[228:229], s[54:55] op_sel_hi:[1,0]
	v_pk_mul_f32 v[230:231], v[230:231], s[54:55] op_sel_hi:[1,0]
	v_pk_mul_f32 v[232:233], v[232:233], s[54:55] op_sel_hi:[1,0]
	v_pk_mul_f32 v[234:235], v[234:235], s[54:55] op_sel_hi:[1,0]
	v_pk_mul_f32 v[228:229], v[80:81], v[228:229]
	v_pk_mul_f32 v[230:231], v[82:83], v[230:231]
	v_pk_mul_f32 v[232:233], v[76:77], v[232:233]
	v_pk_mul_f32 v[234:235], v[78:79], v[234:235]
	v_cvt_pk_bf16_f32 v248, v228, v229
	v_cvt_pk_bf16_f32 v249, v230, v231
	v_cvt_pk_bf16_f32 v250, v232, v233
	v_cvt_pk_bf16_f32 v251, v234, v235
	global_store_dwordx4 v253, v[248:251], s[12:13] offset:256
	v_add_u32_e32 v253, 0x8000, v253
	s_waitcnt vmcnt(15)
	v_cvt_f32_ubyte0_e32 v228, v104
	v_cvt_f32_ubyte1_e32 v229, v104
	v_cvt_f32_ubyte2_e32 v230, v104
	v_cvt_f32_ubyte3_e32 v231, v104
	v_cvt_f32_ubyte0_e32 v232, v105
	v_cvt_f32_ubyte1_e32 v233, v105
	v_cvt_f32_ubyte2_e32 v234, v105
	v_cvt_f32_ubyte3_e32 v235, v105
	v_max_f32_e32 v228, 0x3985b185, v228
	v_max_f32_e32 v229, 0x3985b185, v229
	v_max_f32_e32 v230, 0x3985b185, v230
	v_max_f32_e32 v231, 0x3985b185, v231
	v_max_f32_e32 v232, 0x3985b185, v232
	v_max_f32_e32 v233, 0x3985b185, v233
	v_max_f32_e32 v234, 0x3985b185, v234
	v_max_f32_e32 v235, 0x3985b185, v235
	v_pk_mul_f32 v[228:229], v[228:229], s[54:55] op_sel_hi:[1,0]
	v_pk_mul_f32 v[230:231], v[230:231], s[54:55] op_sel_hi:[1,0]
	v_pk_mul_f32 v[232:233], v[232:233], s[54:55] op_sel_hi:[1,0]
	v_pk_mul_f32 v[234:235], v[234:235], s[54:55] op_sel_hi:[1,0]
	v_pk_mul_f32 v[228:229], v[64:65], v[228:229]
	v_pk_mul_f32 v[230:231], v[66:67], v[230:231]
	v_pk_mul_f32 v[232:233], v[60:61], v[232:233]
	v_pk_mul_f32 v[234:235], v[62:63], v[234:235]
	v_cvt_pk_bf16_f32 v244, v228, v229
	v_cvt_pk_bf16_f32 v245, v230, v231
	v_cvt_pk_bf16_f32 v246, v232, v233
	v_cvt_pk_bf16_f32 v247, v234, v235
	global_store_dwordx4 v253, v[244:247], s[12:13]
	s_waitcnt vmcnt(15)
; __device__ __forceinline__ u32x4 pack8(const f32x4 a, const f32x4 b) { u32x4 w; w.x = cvt_pk_bf16(a[0], a[1]); w.y = cvt_pk_bf16(a[2], a[3]); w.z = cvt_pk_bf16(b[0], b[1]); w.w = cvt_pk_bf16(b[2], b[3]); return w; }
;     __device__ __forceinline__ void operator()(f32x4 (&acc)[2][2][4][2], const Unit& u, int wr, int wc, int fr, int fq) const {
;     ...
;                 for (int bj = 0; bj < 2; ++bj) { const u32x2 a2 = ga[c & 1][m2][bj], b2 = gb[c & 1][m2][bj]; const float q = 1.0f / 255.0f;
;                     const f32x4 sa0 = {(float)((a2.x >> 0) & 0xffu), (float)((a2.x >> 8) & 0xffu), (float)((a2.x >> 16) & 0xffu), (float)((a2.x >> 24) & 0xffu)};
;                     const f32x4 sa1 = {(float)((a2.y >> 0) & 0xffu), (float)((a2.y >> 8) & 0xffu), (float)((a2.y >> 16) & 0xffu), (float)((a2.y >> 24) & 0xffu)};
;                     f32x4 sb0 = {(float)((b2.x >> 0) & 0xffu), (float)((b2.x >> 8) & 0xffu), (float)((b2.x >> 16) & 0xffu), (float)((b2.x >> 24) & 0xffu)};
;                     f32x4 sb1 = {(float)((b2.y >> 0) & 0xffu), (float)((b2.y >> 8) & 0xffu), (float)((b2.y >> 16) & 0xffu), (float)((b2.y >> 24) & 0xffu)};
; #pragma unroll
;                     for (int e = 0; e < 4; ++e) { sb0[e] = fmaxf(sb0[e], 2.55e-4f); sb1[e] = fmaxf(sb1[e], 2.55e-4f); }
;                     if (second) *(u32x4*)(MERGED + (size_t)(row0 + ai * HALF + m * 16) * DM + col0 + bj * HALF) = pack8(acc[ai][bj][m][0] * (sb0 * q), acc[ai][bj][m][1] * (sb1 * q));
	v_cvt_f32_ubyte0_e32 v228, v106
	v_cvt_f32_ubyte1_e32 v229, v106
	v_cvt_f32_ubyte2_e32 v230, v106
	v_cvt_f32_ubyte3_e32 v231, v106
	v_cvt_f32_ubyte0_e32 v232, v107
	v_cvt_f32_ubyte1_e32 v233, v107
	v_cvt_f32_ubyte2_e32 v234, v107
	v_cvt_f32_ubyte3_e32 v235, v107
	v_max_f32_e32 v228, 0x3985b185, v228
	v_max_f32_e32 v229, 0x3985b185, v229
	v_max_f32_e32 v230, 0x3985b185, v230
	v_max_f32_e32 v231, 0x3985b185, v231
	v_max_f32_e32 v232, 0x3985b185, v232
	v_max_f32_e32 v233, 0x3985b185, v233
	v_max_f32_e32 v234, 0x3985b185, v234
	v_max_f32_e32 v235, 0x3985b185, v235
	v_pk_mul_f32 v[228:229], v[228:229], s[54:55] op_sel_hi:[1,0]
	v_pk_mul_f32 v[230:231], v[230:231], s[54:55] op_sel_hi:[1,0]
	v_pk_mul_f32 v[232:233], v[232:233], s[54:55] op_sel_hi:[1,0]
	v_pk_mul_f32 v[234:235], v[234:235], s[54:55] op_sel_hi:[1,0]
	v_pk_mul_f32 v[228:229], v[48:49], v[228:229]
	v_pk_mul_f32 v[230:231], v[50:51], v[230:231]
	v_pk_mul_f32 v[232:233], v[44:45], v[232:233]
	v_pk_mul_f32 v[234:235], v[46:47], v[234:235]
	v_cvt_pk_bf16_f32 v248, v228, v229
	v_cvt_pk_bf16_f32 v249, v230, v231
	v_cvt_pk_bf16_f32 v250, v232, v233
	v_cvt_pk_bf16_f32 v251, v234, v235
	global_store_dwordx4 v253, v[248:251], s[12:13] offset:256
	v_add_u32_e32 v253, 0x8000, v253
	s_waitcnt vmcnt(15)
	v_cvt_f32_ubyte0_e32 v228, v132
	v_cvt_f32_ubyte1_e32 v229, v132
	v_cvt_f32_ubyte2_e32 v230, v132
	v_cvt_f32_ubyte3_e32 v231, v132
	v_cvt_f32_ubyte0_e32 v232, v133
	v_cvt_f32_ubyte1_e32 v233, v133
	v_cvt_f32_ubyte2_e32 v234, v133
	v_cvt_f32_ubyte3_e32 v235, v133
	v_max_f32_e32 v228, 0x3985b185, v228
	v_max_f32_e32 v229, 0x3985b185, v229
	v_max_f32_e32 v230, 0x3985b185, v230
	v_max_f32_e32 v231, 0x3985b185, v231
	v_max_f32_e32 v232, 0x3985b185, v232
	v_max_f32_e32 v233, 0x3985b185, v233
	v_max_f32_e32 v234, 0x3985b185, v234
	v_max_f32_e32 v235, 0x3985b185, v235
	v_pk_mul_f32 v[228:229], v[228:229], s[54:55] op_sel_hi:[1,0]
	v_pk_mul_f32 v[230:231], v[230:231], s[54:55] op_sel_hi:[1,0]
	v_pk_mul_f32 v[232:233], v[232:233], s[54:55] op_sel_hi:[1,0]
	v_pk_mul_f32 v[234:235], v[234:235], s[54:55] op_sel_hi:[1,0]
	v_pk_mul_f32 v[228:229], v[32:33], v[228:229]
	v_pk_mul_f32 v[230:231], v[34:35], v[230:231]
	v_pk_mul_f32 v[232:233], v[28:29], v[232:233]
	v_pk_mul_f32 v[234:235], v[30:31], v[234:235]
	v_cvt_pk_bf16_f32 v244, v228, v229
	v_cvt_pk_bf16_f32 v245, v230, v231
	v_cvt_pk_bf16_f32 v246, v232, v233
	v_cvt_pk_bf16_f32 v247, v234, v235
	global_store_dwordx4 v253, v[244:247], s[12:13]
	s_waitcnt vmcnt(15)
	v_cvt_f32_ubyte0_e32 v228, v134
	v_cvt_f32_ubyte1_e32 v229, v134
	v_cvt_f32_ubyte2_e32 v230, v134
	v_cvt_f32_ubyte3_e32 v231, v134
	v_cvt_f32_ubyte0_e32 v232, v135
	v_cvt_f32_ubyte1_e32 v233, v135
	v_cvt_f32_ubyte2_e32 v234, v135
	v_cvt_f32_ubyte3_e32 v235, v135
	v_max_f32_e32 v228, 0x3985b185, v228
	v_max_f32_e32 v229, 0x3985b185, v229
	v_max_f32_e32 v230, 0x3985b185, v230
	v_max_f32_e32 v231, 0x3985b185, v231
	v_max_f32_e32 v232, 0x3985b185, v232
	v_max_f32_e32 v233, 0x3985b185, v233
	v_max_f32_e32 v234, 0x3985b185, v234
	v_max_f32_e32 v235, 0x3985b185, v235
	v_pk_mul_f32 v[228:229], v[228:229], s[54:55] op_sel_hi:[1,0]
	v_pk_mul_f32 v[230:231], v[230:231], s[54:55] op_sel_hi:[1,0]
	v_pk_mul_f32 v[232:233], v[232:233], s[54:55] op_sel_hi:[1,0]
	v_pk_mul_f32 v[234:235], v[234:235], s[54:55] op_sel_hi:[1,0]
	v_pk_mul_f32 v[228:229], v[24:25], v[228:229]
	v_pk_mul_f32 v[230:231], v[26:27], v[230:231]
	v_pk_mul_f32 v[232:233], v[20:21], v[232:233]
	v_pk_mul_f32 v[234:235], v[22:23], v[234:235]
	v_cvt_pk_bf16_f32 v248, v228, v229
	v_cvt_pk_bf16_f32 v249, v230, v231
	v_cvt_pk_bf16_f32 v250, v232, v233
	v_cvt_pk_bf16_f32 v251, v234, v235
	global_store_dwordx4 v253, v[248:251], s[12:13] offset:256
	v_add_u32_e32 v253, 0x8000, v253
	s_waitcnt vmcnt(15)
	v_cvt_f32_ubyte0_e32 v228, v136
	v_cvt_f32_ubyte1_e32 v229, v136
	v_cvt_f32_ubyte2_e32 v230, v136
	v_cvt_f32_ubyte3_e32 v231, v136
	v_cvt_f32_ubyte0_e32 v232, v137
	v_cvt_f32_ubyte1_e32 v233, v137
	v_cvt_f32_ubyte2_e32 v234, v137
	v_cvt_f32_ubyte3_e32 v235, v137
	v_max_f32_e32 v228, 0x3985b185, v228
	v_max_f32_e32 v229, 0x3985b185, v229
	v_max_f32_e32 v230, 0x3985b185, v230
	v_max_f32_e32 v231, 0x3985b185, v231
	v_max_f32_e32 v232, 0x3985b185, v232
	v_max_f32_e32 v233, 0x3985b185, v233
	v_max_f32_e32 v234, 0x3985b185, v234
	v_max_f32_e32 v235, 0x3985b185, v235
	v_pk_mul_f32 v[228:229], v[228:229], s[54:55] op_sel_hi:[1,0]
	v_pk_mul_f32 v[230:231], v[230:231], s[54:55] op_sel_hi:[1,0]
	v_pk_mul_f32 v[232:233], v[232:233], s[54:55] op_sel_hi:[1,0]
	v_pk_mul_f32 v[234:235], v[234:235], s[54:55] op_sel_hi:[1,0]
	v_pk_mul_f32 v[228:229], v[16:17], v[228:229]
	v_pk_mul_f32 v[230:231], v[18:19], v[230:231]
	v_pk_mul_f32 v[232:233], v[12:13], v[232:233]
	v_pk_mul_f32 v[234:235], v[14:15], v[234:235]
	v_cvt_pk_bf16_f32 v244, v228, v229
	v_cvt_pk_bf16_f32 v245, v230, v231
	v_cvt_pk_bf16_f32 v246, v232, v233
	v_cvt_pk_bf16_f32 v247, v234, v235
	global_store_dwordx4 v253, v[244:247], s[12:13]
	s_waitcnt vmcnt(15)
	v_cvt_f32_ubyte0_e32 v228, v138
	v_cvt_f32_ubyte1_e32 v229, v138
	v_cvt_f32_ubyte2_e32 v230, v138
	v_cvt_f32_ubyte3_e32 v231, v138
	v_cvt_f32_ubyte0_e32 v232, v139
	v_cvt_f32_ubyte1_e32 v233, v139
	v_cvt_f32_ubyte2_e32 v234, v139
	v_cvt_f32_ubyte3_e32 v235, v139
	v_max_f32_e32 v228, 0x3985b185, v228
	v_max_f32_e32 v229, 0x3985b185, v229
	v_max_f32_e32 v230, 0x3985b185, v230
	v_max_f32_e32 v231, 0x3985b185, v231
	v_max_f32_e32 v232, 0x3985b185, v232
	v_max_f32_e32 v233, 0x3985b185, v233
	v_max_f32_e32 v234, 0x3985b185, v234
	v_max_f32_e32 v235, 0x3985b185, v235
	v_pk_mul_f32 v[228:229], v[228:229], s[54:55] op_sel_hi:[1,0]
	v_pk_mul_f32 v[230:231], v[230:231], s[54:55] op_sel_hi:[1,0]
	v_pk_mul_f32 v[232:233], v[232:233], s[54:55] op_sel_hi:[1,0]
	v_pk_mul_f32 v[234:235], v[234:235], s[54:55] op_sel_hi:[1,0]
	v_pk_mul_f32 v[228:229], v[8:9], v[228:229]
	v_pk_mul_f32 v[230:231], v[10:11], v[230:231]
	v_pk_mul_f32 v[232:233], v[4:5], v[232:233]
	v_pk_mul_f32 v[234:235], v[6:7], v[234:235]
	v_cvt_pk_bf16_f32 v248, v228, v229
	v_cvt_pk_bf16_f32 v249, v230, v231
	v_cvt_pk_bf16_f32 v250, v232, v233
	v_cvt_pk_bf16_f32 v251, v234, v235
	global_store_dwordx4 v253, v[248:251], s[12:13] offset:256
.Lmg_end:
.LBB0_1202:
	s_nop 0
	s_andn2_b64 vcc, exec, s[60:61]
	s_mov_b64 s[0:1], -1
	s_cbranch_vccnz .LBB0_1127
	s_andn2_b64 vcc, exec, s[8:9]
	s_cbranch_vccnz .LBB0_1126
	s_barrier
	s_branch .LBB0_1126
